# G=200 (9 GEMM-in rounds): W1 tiles 6400..8191 converted inside GEMM-in epilogues, W2 9088.. inside GEMM1 epilogues, dedicated converters do W1 0..6399
# speedup vs baseline: 1.0191x; 1.0062x over previous
.LBB0_86:
	s_cmp_lt_i32 s50, 2
	s_cselect_b64 s[6:7], -1, 0
	s_and_b64 s[0:1], s[6:7], s[2:3]
	s_andn2_b64 vcc, exec, s[0:1]
	v_writelane_b32 v254, s60, 4
	s_cbranch_vccnz .LBB0_260
	s_mov_b64 s[2:3], s[80:81]
	s_load_dwordx2 s[8:9], s[2:3], 0xa8
	s_cmpk_lg_i32 s56, 0x100
	s_cselect_b32 s0, s56, 0xc8
	s_cmp_ge_i32 s78, s0
	s_mov_b64 s[4:5], -1
	s_cbranch_scc0 .LBB0_145
	s_sub_i32 s1, s78, s0
	s_cmpk_gt_i32 s1, 0x18ff
	s_cbranch_scc1 .LBB0_144
	s_sub_i32 s20, s56, s0
	s_abs_i32 s4, s20
	v_cvt_f32_u32_e32 v1, s4
	s_load_dwordx2 s[10:11], s[2:3], 0x78
	s_load_dwordx2 s[12:13], s[2:3], 0x88
	s_sub_i32 s2, s20, s1
	s_add_i32 s3, s2, 0x18ff
	v_rcp_iflag_f32_e32 v1, v1
	s_sub_i32 s2, 0xffffe701, s2
	s_xor_b32 s14, s3, s20
	s_sub_i32 s5, 0, s4
	v_mul_f32_e32 v1, 0x4f7ffffe, v1
	v_cvt_u32_f32_e32 v1, v1
	s_max_i32 s2, s3, s2
	s_ashr_i32 s3, s14, 31
	v_readfirstlane_b32 s14, v1
	s_mul_i32 s5, s5, s14
	s_mul_hi_u32 s5, s14, s5
	s_add_i32 s14, s14, s5
	s_mul_hi_u32 s5, s2, s14
	s_mul_i32 s14, s5, s4
	s_sub_i32 s2, s2, s14
	s_add_i32 s14, s5, 1
	s_sub_i32 s15, s2, s4
	s_cmp_ge_u32 s2, s4
	s_cselect_b32 s5, s14, s5
	s_cselect_b32 s2, s15, s2
	s_add_i32 s14, s5, 1
	s_cmp_ge_u32 s2, s4
	s_cselect_b32 s2, s14, s5
	s_xor_b32 s2, s2, s3
	s_sub_i32 s29, s2, s3
	s_lshl_b32 s21, s29, 2
	s_add_i32 s22, s21, -1
	s_cmp_gt_i32 s29, 0
	s_cselect_b64 s[2:3], -1, 0
	s_and_b64 s[4:5], s[2:3], exec
	s_cselect_b32 s18, 0, s22
	s_ashr_i32 s4, s18, 2
	s_mul_i32 s17, s4, s20
	s_add_i32 s17, s17, s1
	s_cmpk_gt_i32 s17, 0x1fff
	s_mov_b32 s5, 0
	s_cbranch_scc0 .LBB0_91
	s_add_i32 s4, s17, 0xffffe000
	s_lshr_b32 s4, s4, 7
	s_lshl_b64 s[4:5], s[4:5], 24
	s_waitcnt lgkmcnt(0)
	s_add_u32 s14, s12, s4
	s_addc_u32 s15, s13, s5
	s_lshl_b32 s4, s17, 4
	s_and_b32 s26, s4, 0x780
	s_lshl_b32 s4, s17, 8
	s_and_b32 s16, s4, 0x700
	s_mov_b64 s[4:5], 0x800
	s_cbranch_execz .LBB0_92
	s_branch .LBB0_93

.LBB0_151:
	s_load_dwordx2 s[82:83], s[80:81], 0x78
	v_and_b32_e32 v245, 7, v162
	v_lshrrev_b32_e32 v246, 3, v162
	v_lshlrev_b32_e32 v244, 5, v245
	v_lshl_add_u32 v244, v246, 2, v244
	v_lshlrev_b32_e32 v247, 4, v245
	v_lshl_add_u32 v245, v246, 18, v247
	v_lshl_add_u32 v246, v246, 12, v247
	v_mov_b32_e32 v248, 0x42000000
	v_mov_b32_e32 v249, 0x42000000
	s_waitcnt lgkmcnt(0)
	s_add_u32 s8, s8, 0x6600000
	s_addc_u32 s9, s9, 0
	s_lshl_b32 s3, s3, 5
	s_add_i32 s60, s21, 0x18000
	s_mov_b64 s[10:11], 0x80
	s_and_b32 s3, s3, 0x60
	v_lshl_add_u64 v[8:9], v[8:9], 0, s[10:11]
	s_mov_b32 m0, s60
	s_add_i32 s61, s21, 0x1a000
	s_lshl_b32 s14, s2, 13
	s_lshl_b32 s13, s3, 7
	s_waitcnt vmcnt(2)
	s_barrier
	global_load_lds_dwordx4 v[8:9], off
	v_lshl_add_u64 v[6:7], v[6:7], 0, s[10:11]
	s_mov_b32 m0, s61
	s_add_i32 s62, s21, 0x8000
	s_add_i32 s63, s21, 0xa000
	global_load_lds_dwordx4 v[6:7], off
	v_lshl_add_u64 v[2:3], v[2:3], 0, s[10:11]
	s_mov_b32 m0, s62
	s_add_u32 s28, s44, 0x80080
	global_load_lds_dwordx4 v[2:3], off
	v_lshl_add_u64 v[2:3], v[4:5], 0, s[10:11]
	s_mov_b32 m0, s63
	s_addc_u32 s29, s45, 0
	s_add_i32 s64, s21, 0x1c000
	global_load_lds_dwordx4 v[2:3], off
	v_lshl_add_u64 v[2:3], s[28:29], 0, v[130:131]
	s_mov_b32 m0, s64
	s_add_i32 s65, s21, 0x1e000
	global_load_lds_dwordx4 v[2:3], off
	v_lshl_add_u64 v[2:3], s[28:29], 0, v[136:137]
	s_mov_b32 m0, s65
	v_lshlrev_b32_e32 v4, 6, v0
	global_load_lds_dwordx4 v[2:3], off
	v_and_b32_e32 v2, 15, v0
	v_lshl_or_b32 v1, s2, 6, v2
	v_lshlrev_b32_e32 v3, 1, v13
	s_movk_i32 s2, 0x3c0
	v_lshl_or_b32 v2, v2, 6, v3
	v_and_or_b32 v3, v4, s2, v3
	v_lshlrev_b32_e32 v4, 2, v0
	v_and_b32_e32 v4, 32, v4
	s_add_i32 s2, s13, 0
	v_xad_u32 v3, v3, v4, s2
	v_add_u32_e32 v158, 0x10000, v3
	v_add_u32_e32 v159, 0x14000, v3
	v_add_u32_e32 v160, 0x18000, v3
	v_add_u32_e32 v161, 0x1c000, v3
	v_add_u32_e32 v163, 0x10400, v3
	v_add_u32_e32 v164, 0x10800, v3
	v_add_u32_e32 v165, 0x10c00, v3
	v_add_u32_e32 v166, 0x14400, v3
	v_add_u32_e32 v167, 0x14800, v3
	v_add_u32_e32 v168, 0x14c00, v3
	v_add_u32_e32 v169, 0x18400, v3
	v_add_u32_e32 v170, 0x18800, v3
	v_add_u32_e32 v171, 0x18c00, v3
	v_add_u32_e32 v172, 0x1c400, v3
	v_add_u32_e32 v173, 0x1c800, v3
	v_add_u32_e32 v174, 0x1cc00, v3
	v_lshlrev_b32_e32 v3, 9, v0
	v_xad_u32 v2, v2, v4, 0
	v_and_b32_e32 v3, 0x30000, v3
	v_lshlrev_b32_e32 v4, 12, v12
	v_or3_b32 v3, v10, v3, v4
	v_add_u32_e32 v3, v3, v11
	v_or_b32_e32 v142, 0x80000, v3
	v_lshlrev_b32_e32 v3, 5, v14
	v_and_b32_e32 v3, 0x70000, v3
	s_waitcnt vmcnt(6)
	v_or3_b32 v3, v10, v3, v4
	s_cmpk_lt_u32 s12, 0x100
	v_add_u32_e32 v3, v3, v11
	v_mov_b32_e32 v135, v131
	v_mov_b32_e32 v141, v131
	s_cselect_b64 s[12:13], -1, 0
	s_ashr_i32 s66, s0, 31
	s_ashr_i32 s67, s78, 31
	v_or_b32_e32 v175, s3, v13
	v_mov_b32_e32 v143, v131
	v_or_b32_e32 v144, 0x80000, v3
	v_mov_b32_e32 v145, v131
	v_mov_b64_e32 v[146:147], 0x700
	v_mov_b64_e32 v[148:149], 0x6ff
	s_movk_i32 s68, 0xe1
	v_add_u32_e32 v176, s14, v2
	s_mov_b32 s14, 0x3e6d3388
	s_mov_b32 s16, 0x3f07dc22
	s_mov_b32 s18, 0xbf3a00e3
	s_mov_b32 s20, 0x3f35f0e3
	s_mov_b32 s22, 0xbe11a98e
	s_mov_b32 s24, 0x3e027906
	s_mov_b32 s26, 0xbf38aa3b
	s_movk_i32 s69, 0x3800
	s_barrier
	s_branch .LBB0_154

.LBB0_160:
	s_add_i32 s89, s59, -1
	s_cmp_lt_u32 s89, 9
	s_cselect_b32 s88, 1, 0
	s_cbranch_scc0 .Lp1c_skip1
	s_mul_i32 s89, s89, 200
	s_add_u32 s89, s89, s78
	s_add_u32 s89, s89, 6400
	s_cmp_lt_u32 s89, 0x2000
	s_cselect_b32 s88, 1, 0
	s_cbranch_scc0 .Lp1c_skip1
	s_lshr_b32 s90, s89, 4
	s_lshl_b32 s90, s90, 21
	s_and_b32 s91, s89, 15
	s_lshl_b32 s92, s91, 10
	s_or_b32 s90, s90, s92
	s_lshl_b32 s92, s57, 7
	s_or_b32 s90, s90, s92
	s_add_u32 s84, s82, s90
	s_addc_u32 s85, s83, 0
	s_lshr_b32 s90, s89, 8
	s_lshl_b32 s90, s90, 23
	s_lshl_b32 s91, s91, 19
	s_or_b32 s90, s90, s91
	s_bfe_u32 s91, s89, 0x40004
	s_lshl_b32 s91, s91, 7
	s_or_b32 s90, s90, s91
	s_lshl_b32 s91, s57, 15
	s_or_b32 s90, s90, s91
	s_add_u32 s90, s90, 0x4ee00000
	s_add_u32 s86, s48, s90
	s_addc_u32 s87, s49, 0
	global_load_dwordx4 v[180:183], v245, s[84:85] nt
	s_add_u32 s84, s84, 0x4000
	s_addc_u32 s85, s85, 0
	global_load_dwordx4 v[184:187], v245, s[84:85] nt
	s_add_u32 s84, s84, 0x4000
	s_addc_u32 s85, s85, 0
	global_load_dwordx4 v[188:191], v245, s[84:85] nt
	s_add_u32 s84, s84, 0x4000
	s_addc_u32 s85, s85, 0
	global_load_dwordx4 v[192:195], v245, s[84:85] nt
	s_add_u32 s84, s84, 0x4000
	s_addc_u32 s85, s85, 0
	global_load_dwordx4 v[196:199], v245, s[84:85] nt
	s_add_u32 s84, s84, 0x4000
	s_addc_u32 s85, s85, 0
	global_load_dwordx4 v[200:203], v245, s[84:85] nt
	s_add_u32 s84, s84, 0x4000
	s_addc_u32 s85, s85, 0
	global_load_dwordx4 v[204:207], v245, s[84:85] nt
	s_add_u32 s84, s84, 0x4000
	s_addc_u32 s85, s85, 0
	global_load_dwordx4 v[208:211], v245, s[84:85] nt
	s_add_u32 s84, s84, 0x4000
	s_addc_u32 s85, s85, 0
	global_load_dwordx4 v[212:215], v245, s[84:85] nt
	s_add_u32 s84, s84, 0x4000
	s_addc_u32 s85, s85, 0
	global_load_dwordx4 v[216:219], v245, s[84:85] nt
	s_add_u32 s84, s84, 0x4000
	s_addc_u32 s85, s85, 0
	global_load_dwordx4 v[220:223], v245, s[84:85] nt
	s_add_u32 s84, s84, 0x4000
	s_addc_u32 s85, s85, 0
	global_load_dwordx4 v[224:227], v245, s[84:85] nt
	s_add_u32 s84, s84, 0x4000
	s_addc_u32 s85, s85, 0
	global_load_dwordx4 v[228:231], v245, s[84:85] nt
	s_add_u32 s84, s84, 0x4000
	s_addc_u32 s85, s85, 0
	global_load_dwordx4 v[232:235], v245, s[84:85] nt
	s_add_u32 s84, s84, 0x4000
	s_addc_u32 s85, s85, 0
	global_load_dwordx4 v[236:239], v245, s[84:85] nt
	s_add_u32 s84, s84, 0x4000
	s_addc_u32 s85, s85, 0
	global_load_dwordx4 v[240:243], v245, s[84:85] nt

.LBB0_256:
	s_andn2_b64 vcc, exec, s[2:3]
	s_mov_b64 s[2:3], -1
	v_cvt_pk_bf16_f32 v2, v14, v15
	v_cvt_pk_bf16_f32 v3, v12, v13
	v_cvt_pk_bf16_f32 v4, v18, v19
	v_cvt_pk_bf16_f32 v5, v16, v17
	global_store_dwordx4 v[10:11], v[2:5], off offset:256
	s_cmp_eq_u32 s88, 0
	s_cbranch_scc1 .Lp1c_skip3
	s_waitcnt vmcnt(16)
	v_pk_mul_f32 v[180:181], v[180:181], v[248:249]
	v_pk_mul_f32 v[182:183], v[182:183], v[248:249]
	v_pk_mul_f32 v[184:185], v[184:185], v[248:249]
	v_pk_mul_f32 v[186:187], v[186:187], v[248:249]
	v_pk_mul_f32 v[188:189], v[188:189], v[248:249]
	v_pk_mul_f32 v[190:191], v[190:191], v[248:249]
	v_pk_mul_f32 v[192:193], v[192:193], v[248:249]
	v_pk_mul_f32 v[194:195], v[194:195], v[248:249]
	v_pk_mul_f32 v[196:197], v[196:197], v[248:249]
	v_pk_mul_f32 v[198:199], v[198:199], v[248:249]
	v_pk_mul_f32 v[200:201], v[200:201], v[248:249]
	v_pk_mul_f32 v[202:203], v[202:203], v[248:249]
	v_pk_mul_f32 v[204:205], v[204:205], v[248:249]
	v_pk_mul_f32 v[206:207], v[206:207], v[248:249]
	v_pk_mul_f32 v[208:209], v[208:209], v[248:249]
	v_pk_mul_f32 v[210:211], v[210:211], v[248:249]
	v_pk_mul_f32 v[212:213], v[212:213], v[248:249]
	v_pk_mul_f32 v[214:215], v[214:215], v[248:249]
	v_pk_mul_f32 v[216:217], v[216:217], v[248:249]
	v_pk_mul_f32 v[218:219], v[218:219], v[248:249]
	v_pk_mul_f32 v[220:221], v[220:221], v[248:249]
	v_pk_mul_f32 v[222:223], v[222:223], v[248:249]
	v_pk_mul_f32 v[224:225], v[224:225], v[248:249]
	v_pk_mul_f32 v[226:227], v[226:227], v[248:249]
	v_pk_mul_f32 v[228:229], v[228:229], v[248:249]
	v_pk_mul_f32 v[230:231], v[230:231], v[248:249]
	v_pk_mul_f32 v[232:233], v[232:233], v[248:249]
	v_pk_mul_f32 v[234:235], v[234:235], v[248:249]
	v_pk_mul_f32 v[236:237], v[236:237], v[248:249]
	v_pk_mul_f32 v[238:239], v[238:239], v[248:249]
	v_pk_mul_f32 v[240:241], v[240:241], v[248:249]
	v_pk_mul_f32 v[242:243], v[242:243], v[248:249]
	v_cvt_pk_fp8_f32 v34, v180, v184
	v_cvt_pk_fp8_f32 v35, v196, v200
	v_cvt_pk_fp8_f32 v36, v212, v216
	v_cvt_pk_fp8_f32 v37, v228, v232
	v_cvt_pk_fp8_f32 v34, v188, v192 op_sel:[0,0,1]
	v_cvt_pk_fp8_f32 v35, v204, v208 op_sel:[0,0,1]
	v_cvt_pk_fp8_f32 v36, v220, v224 op_sel:[0,0,1]
	v_cvt_pk_fp8_f32 v37, v236, v240 op_sel:[0,0,1]
	v_cvt_pk_fp8_f32 v38, v181, v185
	v_cvt_pk_fp8_f32 v39, v197, v201
	v_cvt_pk_fp8_f32 v40, v213, v217
	v_cvt_pk_fp8_f32 v41, v229, v233
	v_cvt_pk_fp8_f32 v38, v189, v193 op_sel:[0,0,1]
	v_cvt_pk_fp8_f32 v39, v205, v209 op_sel:[0,0,1]
	v_cvt_pk_fp8_f32 v40, v221, v225 op_sel:[0,0,1]
	v_cvt_pk_fp8_f32 v41, v237, v241 op_sel:[0,0,1]
	v_cvt_pk_fp8_f32 v42, v182, v186
	v_cvt_pk_fp8_f32 v43, v198, v202
	v_cvt_pk_fp8_f32 v44, v214, v218
	v_cvt_pk_fp8_f32 v45, v230, v234
	v_cvt_pk_fp8_f32 v42, v190, v194 op_sel:[0,0,1]
	v_cvt_pk_fp8_f32 v43, v206, v210 op_sel:[0,0,1]
	v_cvt_pk_fp8_f32 v44, v222, v226 op_sel:[0,0,1]
	v_cvt_pk_fp8_f32 v45, v238, v242 op_sel:[0,0,1]
	v_cvt_pk_fp8_f32 v46, v183, v187
	v_cvt_pk_fp8_f32 v47, v199, v203
	v_cvt_pk_fp8_f32 v48, v215, v219
	v_cvt_pk_fp8_f32 v49, v231, v235
	v_cvt_pk_fp8_f32 v46, v191, v195 op_sel:[0,0,1]
	v_cvt_pk_fp8_f32 v47, v207, v211 op_sel:[0,0,1]
	v_cvt_pk_fp8_f32 v48, v223, v227 op_sel:[0,0,1]
	v_cvt_pk_fp8_f32 v49, v239, v243 op_sel:[0,0,1]
	s_nop 1
	ds_bpermute_b32 v50, v244, v34
	ds_bpermute_b32 v51, v244, v35
	ds_bpermute_b32 v52, v244, v36
	ds_bpermute_b32 v53, v244, v37
	ds_bpermute_b32 v54, v244, v38
	ds_bpermute_b32 v55, v244, v39
	ds_bpermute_b32 v56, v244, v40
	ds_bpermute_b32 v57, v244, v41
	ds_bpermute_b32 v58, v244, v42
	ds_bpermute_b32 v59, v244, v43
	ds_bpermute_b32 v60, v244, v44
	ds_bpermute_b32 v61, v244, v45
	ds_bpermute_b32 v62, v244, v46
	ds_bpermute_b32 v63, v244, v47
	ds_bpermute_b32 v64, v244, v48
	ds_bpermute_b32 v65, v244, v49
	s_waitcnt lgkmcnt(0)
	global_store_dwordx4 v246, v[50:53], s[86:87] nt
	s_add_u32 s90, s86, 0x40000
	s_addc_u32 s91, s87, 0
	global_store_dwordx4 v246, v[54:57], s[90:91] nt
	s_add_u32 s90, s86, 0x800
	s_addc_u32 s91, s87, 0
	global_store_dwordx4 v246, v[58:61], s[90:91] nt
	s_add_u32 s90, s86, 0x40800
	s_addc_u32 s91, s87, 0
	global_store_dwordx4 v246, v[62:65], s[90:91] nt
.Lp1c_skip3:
	s_cbranch_vccnz .LBB0_153
	s_andn2_b64 vcc, exec, s[4:5]
	s_cbranch_vccnz .LBB0_152
	s_barrier
	s_branch .LBB0_152
